# v8
# baseline (speedup 1.0000x reference)
.LBB1_27:
	s_mulk_i32 s31, 0xc0
	s_lshl_b32 s7, s31, 2
	s_lshl_b32 s6, s31, 4
	s_add_i32 s7, s7, 0x16400
	s_add_i32 s6, s6, 0x17000
	s_cmp_eq_u32 s30, 0
	s_cselect_b64 s[2:3], -1, 0
	s_cmp_lg_u32 s30, 0
	s_cselect_b64 s[0:1], -1, 0
	s_and_b64 vcc, exec, s[2:3]
	s_waitcnt lgkmcnt(0)
	s_barrier
	s_cbranch_vccz .LBB1_43
	s_add_i32 s8, s27, 0x15800
	v_mov_b32_e32 v0, s8
	ds_read_b32 v2, v0 offset:60
	ds_read_b32 v3, v0 offset:124
	ds_read_b32 v4, v0 offset:188
	ds_read_b32 v5, v0 offset:252
	ds_read_b32 v6, v0 offset:316
	ds_read_b32 v7, v0 offset:380
	ds_read_b32 v8, v0 offset:444
	ds_read_b32 v9, v0 offset:508
	v_add_u32_e32 v28, s13, v121
	v_lshlrev_b32_e32 v29, 2, v120
	v_add_u32_e32 v30, s8, v29
	v_add_u32_e32 v31, s23, v29
	v_lshl_add_u32 v44, s19, 4, v121
	v_add_u32_e32 v44, 0x13000, v44
	ds_read_b128 v[32:35], v28
	ds_read_b32 v40, v30
	ds_read_b32 v41, v31
	ds_read_b32 v42, v30 offset:256
	ds_read_b32 v43, v31 offset:256
	ds_read_b128 v[36:39], v44
	ds_read_b128 v[48:51], v44 offset:1024
	v_mov_b32_e32 v1, 0
	s_waitcnt lgkmcnt(7)
	v_sub_u32_e32 v10, v2, v120
	v_lshrrev_b32_e32 v10, 31, v10
	v_add_u32_e32 v1, v1, v10
	v_sub_u32_e32 v10, v3, v120
	v_lshrrev_b32_e32 v10, 31, v10
	v_add_u32_e32 v1, v1, v10
	v_sub_u32_e32 v10, v4, v120
	v_lshrrev_b32_e32 v10, 31, v10
	v_add_u32_e32 v1, v1, v10
	v_sub_u32_e32 v10, v5, v120
	v_lshrrev_b32_e32 v10, 31, v10
	v_add_u32_e32 v1, v1, v10
	v_sub_u32_e32 v10, v6, v120
	v_lshrrev_b32_e32 v10, 31, v10
	v_add_u32_e32 v1, v1, v10
	v_sub_u32_e32 v10, v7, v120
	v_lshrrev_b32_e32 v10, 31, v10
	v_add_u32_e32 v1, v1, v10
	v_sub_u32_e32 v10, v8, v120
	v_lshrrev_b32_e32 v10, 31, v10
	v_add_u32_e32 v1, v1, v10
	v_sub_u32_e32 v10, v9, v120
	v_lshrrev_b32_e32 v10, 31, v10
	v_add_u32_e32 v1, v1, v10
	v_min_u32_e32 v1, 7, v1
	v_lshl_add_u32 v10, v1, 6, s8
	ds_read_b128 v[12:15], v10
	ds_read_b128 v[16:19], v10 offset:16
	ds_read_b128 v[20:23], v10 offset:32
	ds_read_b128 v[24:27], v10 offset:48
	v_lshlrev_b32_e32 v1, 4, v1
	s_waitcnt lgkmcnt(0)
	v_sub_u32_e32 v10, v12, v120
	v_lshrrev_b32_e32 v10, 31, v10
	v_add_u32_e32 v1, v1, v10
	v_sub_u32_e32 v10, v13, v120
	v_lshrrev_b32_e32 v10, 31, v10
	v_add_u32_e32 v1, v1, v10
	v_sub_u32_e32 v10, v14, v120
	v_lshrrev_b32_e32 v10, 31, v10
	v_add_u32_e32 v1, v1, v10
	v_sub_u32_e32 v10, v15, v120
	v_lshrrev_b32_e32 v10, 31, v10
	v_add_u32_e32 v1, v1, v10
	v_sub_u32_e32 v10, v16, v120
	v_lshrrev_b32_e32 v10, 31, v10
	v_add_u32_e32 v1, v1, v10
	v_sub_u32_e32 v10, v17, v120
	v_lshrrev_b32_e32 v10, 31, v10
	v_add_u32_e32 v1, v1, v10
	v_sub_u32_e32 v10, v18, v120
	v_lshrrev_b32_e32 v10, 31, v10
	v_add_u32_e32 v1, v1, v10
	v_sub_u32_e32 v10, v19, v120
	v_lshrrev_b32_e32 v10, 31, v10
	v_add_u32_e32 v1, v1, v10
	v_sub_u32_e32 v10, v20, v120
	v_lshrrev_b32_e32 v10, 31, v10
	v_add_u32_e32 v1, v1, v10
	v_sub_u32_e32 v10, v21, v120
	v_lshrrev_b32_e32 v10, 31, v10
	v_add_u32_e32 v1, v1, v10
	v_sub_u32_e32 v10, v22, v120
	v_lshrrev_b32_e32 v10, 31, v10
	v_add_u32_e32 v1, v1, v10
	v_sub_u32_e32 v10, v23, v120
	v_lshrrev_b32_e32 v10, 31, v10
	v_add_u32_e32 v1, v1, v10
	v_sub_u32_e32 v10, v24, v120
	v_lshrrev_b32_e32 v10, 31, v10
	v_add_u32_e32 v1, v1, v10
	v_sub_u32_e32 v10, v25, v120
	v_lshrrev_b32_e32 v10, 31, v10
	v_add_u32_e32 v1, v1, v10
	v_sub_u32_e32 v10, v26, v120
	v_lshrrev_b32_e32 v10, 31, v10
	v_add_u32_e32 v1, v1, v10
	v_sub_u32_e32 v10, v27, v120
	v_lshrrev_b32_e32 v10, 31, v10
	v_add_u32_e32 v1, v1, v10
	v_add_u32_e32 v4, v1, v120
	v_cvt_f32_ubyte0_e32 v0, v120
	v_fmac_f32_e32 v123, v0, v124
	v_lshl_add_u32 v0, v4, 2, s7
	ds_write_b32 v0, v123
	v_lshl_add_u32 v4, v4, 4, s6
	ds_write_b128 v4, v[32:35]
	v_add_u32_e32 v6, v120, v40
	v_lshl_add_u32 v1, v6, 2, s7
	ds_write_b32 v1, v41 offset:4
	v_lshl_add_u32 v6, v6, 4, s6
	ds_write_b128 v6, v[36:39] offset:16
	v_add_u32_e32 v5, v120, v42
	v_lshl_add_u32 v0, v5, 2, s7
	ds_write_b32 v0, v43 offset:260
	v_lshl_add_u32 v5, v5, 4, s6
	ds_write_b128 v5, v[48:51] offset:1040
